# v6 + ss_scan units moved off the ctx-attention blocks (layer 0) + the two routing atomics of a token issued together
# baseline (speedup 1.0000x reference)
.LBB0_967:
	s_add_i32 s0, s2, 0xc0
	s_ashr_i32 s1, s0, 31
	s_abs_i32 s0, s0
	s_mul_hi_u32 s4, s0, s53
	s_mul_i32 s4, s4, s52
	s_sub_i32 s0, s0, s4
	s_sub_i32 s4, s0, s52
	s_cmp_ge_u32 s0, s52
	s_cselect_b32 s0, s4, s0
	s_sub_i32 s4, s0, s52
	s_cmp_ge_u32 s0, s52
	s_cselect_b32 s0, s4, s0
	s_xor_b32 s0, s0, s1
	s_sub_i32 s38, s0, s1
	s_cmpk_lt_i32 s38, 0x80
	s_cselect_b64 s[0:1], -1, 0
	s_add_u32 s39, s26, 0x50610000
	s_addc_u32 s40, s27, 0
	s_add_u32 s41, s26, 0x5bd00000
	s_addc_u32 s42, s27, 0
	s_add_u32 s43, s26, 0x57500000
	s_addc_u32 s44, s27, 0
	v_readlane_b32 s4, v246, 18
	s_bitcmp1_b32 s4, 7
	v_cndmask_b32_e64 v2, 0, 1, s[0:1]
	s_cselect_b64 s[4:5], -1, 0
	v_cmp_ne_u32_e64 s[0:1], 1, v2
	s_movk_i32 s45, 0x1000
	s_mov_b32 s7, 0
	v_mov_b32_e32 v7, 0
	s_movk_i32 s46, 0x3000
	s_movk_i32 s47, 0x2000
	s_branch .LBB0_969

.LBB0_3677:
	s_or_b64 exec, exec, s[8:9]
	v_sub_f32_e32 v37, v37, v38
	v_mul_f32_e32 v38, 0x3fb8aa3b, v37
	v_fma_f32 v41, v37, s41, -v38
	v_rndne_f32_e32 v42, v38
	v_fmac_f32_e32 v41, 0x32a5705f, v37
	v_sub_f32_e32 v38, v38, v42
	v_add_f32_e32 v38, v38, v41
	v_cvt_i32_f32_e32 v41, v42
	v_exp_f32_e32 v38, v38
	v_cmp_ngt_f32_e32 vcc, s42, v37
	s_waitcnt vmcnt(0)
	v_readfirstlane_b32 s5, v40
	v_readfirstlane_b32 s24, v251
	v_ldexp_f32 v38, v38, v41
	v_cndmask_b32_e32 v38, 0, v38, vcc
	v_cmp_nlt_f32_e32 vcc, s43, v37
	v_add_u32_e32 v39, s5, v39
	v_lshl_add_u32 v138, s4, 13, v39
	v_cndmask_b32_e32 v37, v137, v38, vcc
	v_add_f32_e32 v38, 1.0, v37
	v_div_scale_f32 v41, s[6:7], v38, v38, 1.0
	v_rcp_f32_e32 v42, v41
	v_add_u32_e32 v37, s24, v36
	s_add_u32 s6, s26, s16
	s_addc_u32 s7, s27, s17
	v_fma_f32 v36, -v41, v42, 1.0
	v_fmac_f32_e32 v42, v36, v42
	v_div_scale_f32 v36, vcc, 1.0, v38, 1.0
	v_mul_f32_e32 v43, v36, v42
	v_fma_f32 v44, -v41, v43, v36
	v_fmac_f32_e32 v43, v44, v42
	v_fma_f32 v36, -v41, v43, v36
	v_div_fmas_f32 v36, v36, v42, v43
	v_div_fixup_f32 v43, v36, v38, 1.0
	v_mov_b32_e32 v36, s12
	v_mov_b32_e32 v38, s4
	v_sub_f32_e32 v42, 1.0, v43
	global_store_dwordx4 v134, v[36:39], s[6:7]
	global_store_dwordx2 v134, v[42:43], s[6:7] offset:16
	s_nop 0
	v_lshl_add_u32 v38, s12, 13, v37
	v_mov_b64_e32 v[36:37], 0

.LBB0_3684:
	s_mov_b64 s[8:9], exec
	v_mbcnt_lo_u32_b32 v36, s8, 0
	v_mbcnt_hi_u32_b32 v36, s9, v36
	v_cmp_eq_u32_e32 vcc, 0, v36
	s_and_saveexec_b64 s[6:7], vcc
	s_cbranch_execz .LBB0_3686
	s_lshl_b64 s[24:25], s[12:13], 8
	s_add_u32 s24, s36, s24
	s_addc_u32 s25, s37, s25
	s_bcnt1_i32_b64 s5, s[8:9]
	v_mov_b32_e32 v39, s5
	global_atomic_add v251, v123, v39, s[24:25] sc0
.LBB0_3686:
	s_or_b64 exec, exec, s[6:7]
	s_mov_b64 s[6:7], exec
	v_mbcnt_lo_u32_b32 v39, s6, 0
	v_mbcnt_hi_u32_b32 v39, s7, v39
	v_cmp_eq_u32_e32 vcc, 0, v39
	s_and_saveexec_b64 s[8:9], vcc
	s_cbranch_execz .LBB0_3677
	s_ashr_i32 s5, s4, 31
	s_lshl_b64 s[28:29], s[4:5], 8
	s_add_u32 s28, s36, s28
	s_addc_u32 s29, s37, s29
	s_bcnt1_i32_b64 s5, s[6:7]
	v_mov_b32_e32 v40, s5
	global_atomic_add v40, v123, v40, s[28:29] sc0
	s_branch .LBB0_3677
